# merge GEMM: the LDS-DMA loads of the unused second B half-tile removed, counted waits lowered to match
# speedup vs baseline: 1.0038x; 1.0038x over previous
.LBB0_870:
	s_andn2_b64 vcc, exec, vcc
	s_cbranch_vccnz .LBB0_902
	v_mov_b32_e32 v2, v0
	s_mov_b32 s54, 0x7fffe0
	v_ashrrev_i32_e32 v4, 31, v2
	v_lshrrev_b32_e32 v4, 26, v4
	v_lshlrev_b32_e32 v3, 4, v2
	v_add_u32_e32 v4, v2, v4
	v_bfe_i32 v2, v2, 27, 1
	v_lshrrev_b32_e32 v2, 22, v2
	v_add_u32_e32 v2, v3, v2
	v_and_b32_e32 v2, 0xfffffc00, v2
	v_sub_u32_e32 v2, v3, v2
	v_lshrrev_b32_e32 v5, 4, v2
	v_bitop3_b32 v2, v5, v2, 32 bitop3:0x6c
	v_ashrrev_i32_e32 v6, 31, v2
	v_ashrrev_i32_e32 v4, 6, v4
	v_lshrrev_b32_e32 v6, 26, v6
	v_lshlrev_b32_e32 v5, 3, v4
	v_add_u32_e32 v6, v2, v6
	v_and_b32_e32 v5, -16, v5
	v_ashrrev_i32_e32 v7, 6, v6
	v_and_b32_e32 v6, 0xc0, v6
	v_add_u32_e32 v5, v7, v5
	v_sub_u32_e32 v2, v2, v6
	v_lshlrev_b32_e32 v4, 5, v4
	v_ashrrev_i16_sdwa v2, v231, sext(v2) dst_sel:DWORD dst_unused:UNUSED_PAD src0_sel:DWORD src1_sel:BYTE_0
	v_lshlrev_b32_e32 v6, 1, v5
	v_lshrrev_b32_e32 v8, 2, v5
	v_and_b32_e32 v7, 3, v7
	v_and_b32_e32 v4, 32, v4
	v_bfe_i32 v2, v2, 0, 16
	v_and_b32_e32 v6, 24, v6
	v_and_b32_e32 v8, 4, v8
	v_and_or_b32 v7, v5, s54, v7
	v_or3_b32 v6, v7, v8, v6
	v_add_lshl_u32 v2, v4, v2, 1
	v_lshl_add_u32 v218, v5, 9, v2
	v_lshl_add_u32 v94, v6, 9, v2
	v_add_u32_e32 v2, 0x2000, v3
	v_ashrrev_i32_e32 v3, 31, v2
	v_lshrrev_b32_e32 v3, 22, v3
	v_add_u32_e32 v3, v2, v3
	v_ashrrev_i32_e32 v3, 10, v3
	v_mul_i32_i24_e32 v4, 0x400, v3
	v_sub_u32_e32 v2, v2, v4
	v_lshrrev_b32_e32 v4, 4, v2
	v_bitop3_b32 v2, v4, v2, 32 bitop3:0x6c
	v_ashrrev_i32_e32 v5, 31, v2
	v_lshrrev_b32_e32 v5, 26, v5
	v_lshlrev_b32_e32 v4, 3, v3
	v_add_u32_e32 v5, v2, v5
	v_and_b32_e32 v4, -16, v4
	v_ashrrev_i32_e32 v6, 6, v5
	v_and_b32_e32 v5, 0xc0, v5
	s_ashr_i32 s5, s4, 6
	v_add_u32_e32 v4, v6, v4
	v_sub_u32_e32 v2, v2, v5
	s_lshl_b32 s6, s5, 10
	v_lshlrev_b32_e32 v3, 5, v3
	v_ashrrev_i16_sdwa v2, v231, sext(v2) dst_sel:DWORD dst_unused:UNUSED_PAD src0_sel:DWORD src1_sel:BYTE_0
	v_lshlrev_b32_e32 v5, 1, v4
	v_lshrrev_b32_e32 v7, 2, v4
	v_and_b32_e32 v6, 3, v6
	s_add_i32 s39, s14, 0x10000
	v_and_b32_e32 v3, 32, v3
	v_bfe_i32 v2, v2, 0, 16
	v_and_b32_e32 v5, 24, v5
	v_and_b32_e32 v7, 4, v7
	v_and_or_b32 v6, v4, s54, v6
	s_add_i32 s40, s39, s6
	v_or3_b32 v5, v6, v7, v5
	v_add_lshl_u32 v2, v3, v2, 1
	s_mov_b32 m0, s40
	s_add_i32 s41, s40, 0x2000
	s_add_i32 s42, s14, 0x14000
	v_lshl_add_u32 v98, v5, 9, v2
	global_load_lds_dwordx4 v94, s[26:27]
	s_mov_b32 m0, s41
	s_add_i32 s42, s42, s6
	global_load_lds_dwordx4 v98, s[26:27]
	s_add_i32 s43, s42, 0x2000
	s_add_i32 s44, s14, s6
	s_ashr_i32 s7, s4, 8
	s_add_i32 s45, s44, 0x2000
	s_mov_b32 m0, s44
	s_add_u32 s2, s24, 0x10000
	v_lshl_add_u32 v96, v4, 9, v2
	global_load_lds_dwordx4 v218, s[24:25]
	s_mov_b32 m0, s45
	s_addc_u32 s3, s25, 0
	s_add_i32 s46, s44, 0x4000
	global_load_lds_dwordx4 v96, s[24:25]
	s_mov_b32 m0, s46
	s_add_i32 s47, s44, 0x6000
	global_load_lds_dwordx4 v218, s[2:3]
	s_mov_b32 m0, s47
	v_mov_b32_e32 v95, v219
	global_load_lds_dwordx4 v96, s[2:3]
	v_mov_b32_e32 v99, v219
	v_mov_b32_e32 v97, v219
	s_cmp_eq_u32 s7, 1
	v_lshl_add_u64 v[8:9], s[26:27], 0, v[94:95]
	v_lshl_add_u64 v[6:7], s[26:27], 0, v[98:99]
	v_lshl_add_u64 v[2:3], s[24:25], 0, v[218:219]
	s_cselect_b64 s[2:3], -1, 0
	s_cmp_lg_u32 s7, 1
	v_lshl_add_u64 v[4:5], s[24:25], 0, v[96:97]
	s_cbranch_scc1 .LBB0_873
	s_barrier
.LBB0_873:
	s_add_u32 s10, s8, 0x3c400000
	s_addc_u32 s11, s9, 0
	s_add_u32 s8, s8, 0x56700000
	s_addc_u32 s9, s9, 0
	s_add_i32 s48, s14, 0x18000
	s_add_i32 s49, s48, s6
	v_lshl_add_u64 v[8:9], v[8:9], 0, s[72:73]
	s_mov_b32 m0, s49
	s_add_i32 s50, s49, 0x2000
	s_waitcnt vmcnt(2)
	s_barrier
	global_load_lds_dwordx4 v[8:9], off
	v_lshl_add_u64 v[6:7], v[6:7], 0, s[72:73]
	s_mov_b32 m0, s50
	s_add_i32 s51, s44, 0x8000
	global_load_lds_dwordx4 v[6:7], off
	v_lshl_add_u64 v[2:3], v[2:3], 0, s[72:73]
	s_mov_b32 m0, s51
	s_add_i32 s56, s44, 0xa000
	s_add_i32 s57, s14, 0x1c000
	global_load_lds_dwordx4 v[2:3], off
	v_lshl_add_u64 v[2:3], v[4:5], 0, s[72:73]
	s_mov_b32 m0, s56
	s_add_i32 s57, s57, s6
	global_load_lds_dwordx4 v[2:3], off
	s_add_i32 s58, s57, 0x2000
	v_and_b32_e32 v11, 15, v10
	v_and_b32_e32 v12, 48, v10
	v_lshlrev_b32_e32 v11, 6, v11
	v_lshlrev_b32_e32 v2, 2, v10
	s_lshl_b32 s5, s5, 12
	v_or_b32_e32 v13, v11, v12
	s_lshl_b32 s7, s7, 13
	v_and_b32_e32 v2, 32, v2
	s_and_b32 s5, s5, 0x3000
	s_waitcnt vmcnt(4)
	v_bitop3_b32 v3, v11, v2, v12 bitop3:0x36
	v_bitop3_b32 v2, v13, s7, v2 bitop3:0xde
	s_cmpk_lt_u32 s4, 0x100
	v_mov_b32_e32 v102, 0
	v_or_b32_e32 v182, s5, v3
	s_cselect_b64 s[12:13], -1, 0
	s_ashr_i32 s60, s29, 31
	s_mov_b32 s33, 0
	s_mov_b32 s61, 1
	v_add_u32_e32 v183, s14, v2
	v_mov_b32_e32 v103, v102
	v_mov_b32_e32 v144, v102
	v_mov_b32_e32 v145, v102
	v_mov_b32_e32 v100, v102
	v_mov_b32_e32 v101, v102
	v_mov_b32_e32 v132, v102
	v_mov_b32_e32 v133, v102
	v_mov_b32_e32 v110, v102
	v_mov_b32_e32 v111, v102
	v_mov_b32_e32 v148, v102
	v_mov_b32_e32 v149, v102
	v_mov_b32_e32 v104, v102
	v_mov_b32_e32 v105, v102
	v_mov_b32_e32 v134, v102
	v_mov_b32_e32 v135, v102
	v_mov_b32_e32 v114, v102
	v_mov_b32_e32 v115, v102
	v_mov_b32_e32 v152, v102
	v_mov_b32_e32 v153, v102
	v_mov_b32_e32 v106, v102
	v_mov_b32_e32 v107, v102
	v_mov_b32_e32 v136, v102
	v_mov_b32_e32 v137, v102
	v_mov_b32_e32 v118, v102
	v_mov_b32_e32 v119, v102
	v_mov_b32_e32 v154, v102
	v_mov_b32_e32 v155, v102
	v_mov_b32_e32 v108, v102
	v_mov_b32_e32 v109, v102
	v_mov_b32_e32 v138, v102
	v_mov_b32_e32 v139, v102
	v_mov_b32_e32 v122, v102
	v_mov_b32_e32 v123, v102
	v_mov_b32_e32 v156, v102
	v_mov_b32_e32 v157, v102
	v_mov_b32_e32 v112, v102
	v_mov_b32_e32 v113, v102
	v_mov_b32_e32 v140, v102
	v_mov_b32_e32 v141, v102
	v_mov_b32_e32 v126, v102
	v_mov_b32_e32 v127, v102
	v_mov_b32_e32 v158, v102
	v_mov_b32_e32 v159, v102
	v_mov_b32_e32 v116, v102
	v_mov_b32_e32 v117, v102
	v_mov_b32_e32 v142, v102
	v_mov_b32_e32 v143, v102
	v_mov_b32_e32 v128, v102
	v_mov_b32_e32 v129, v102
	v_mov_b32_e32 v160, v102
	v_mov_b32_e32 v161, v102
	v_mov_b32_e32 v120, v102
	v_mov_b32_e32 v121, v102
	v_mov_b32_e32 v146, v102
	v_mov_b32_e32 v147, v102
	v_mov_b32_e32 v130, v102
	v_mov_b32_e32 v131, v102
	v_mov_b32_e32 v162, v102
	v_mov_b32_e32 v163, v102
	v_mov_b32_e32 v124, v102
	v_mov_b32_e32 v125, v102
	v_mov_b32_e32 v150, v102
	v_mov_b32_e32 v151, v102
	s_barrier
	s_branch .LBB0_876

.LBB0_876:
	v_add_u32_e32 v196, s39, v182
	ds_read_b128 v[2:5], v196
	ds_read_b128 v[6:9], v196 offset:1024
	ds_read_b128 v[10:13], v196 offset:2048
	ds_read_b128 v[14:17], v196 offset:3072
	s_mul_hi_u32 s4, s61, 0xaaaaaaab
	s_lshr_b32 s19, s4, 2
	s_add_u32 s6, s24, 0x10080
	s_addc_u32 s7, s25, 0
	s_add_i32 s4, s44, 0xc000
	s_mov_b32 m0, s4
	s_add_i32 s5, s44, 0xe000
	ds_read_b128 v[22:25], v183
	ds_read_b128 v[26:29], v183 offset:1024
	ds_read_b128 v[30:33], v183 offset:2048
	ds_read_b128 v[34:37], v183 offset:3072
	ds_read_b128 v[38:41], v183 offset:4096
	ds_read_b128 v[42:45], v183 offset:5120
	ds_read_b128 v[82:85], v183 offset:6144
	ds_read_b128 v[86:89], v183 offset:7168
	global_load_lds_dwordx4 v218, s[6:7]
	s_mov_b32 m0, s5
	v_mov_b32_e32 v97, v219
	global_load_lds_dwordx4 v96, s[6:7]
	s_waitcnt vmcnt(6)
	s_waitcnt lgkmcnt(0)
	s_barrier
	s_setprio 1
	v_mov_b64_e32 v[18:19], s[88:89]
	v_mov_b64_e32 v[78:79], s[88:89]
	v_mov_b64_e32 v[74:75], s[88:89]
	v_mov_b64_e32 v[70:71], s[88:89]
	v_mov_b64_e32 v[66:67], s[88:89]
	v_mov_b64_e32 v[62:63], s[88:89]
	v_mov_b64_e32 v[58:59], s[88:89]
	v_mov_b64_e32 v[54:55], s[88:89]
	v_mov_b64_e32 v[50:51], s[88:89]
	v_mov_b64_e32 v[20:21], s[90:91]
	v_mov_b64_e32 v[80:81], s[90:91]
	v_mov_b64_e32 v[76:77], s[90:91]
	v_mov_b64_e32 v[72:73], s[90:91]
	v_mov_b64_e32 v[68:69], s[90:91]
	v_mov_b64_e32 v[64:65], s[90:91]
	v_mov_b64_e32 v[60:61], s[90:91]
	v_mov_b64_e32 v[56:57], s[90:91]
	v_mov_b64_e32 v[52:53], s[90:91]
	s_waitcnt lgkmcnt(0)
	v_mfma_scale_f32_16x16x128_f8f6f4 v[78:81], v[2:9], v[22:29], v[78:81], v232, v232 op_sel_hi:[0,0,0]
	v_mfma_scale_f32_16x16x128_f8f6f4 v[74:77], v[10:17], v[22:29], v[74:77], v232, v232 op_sel_hi:[0,0,0]
	v_mfma_scale_f32_16x16x128_f8f6f4 v[70:73], v[2:9], v[30:37], v[70:73], v232, v232 op_sel_hi:[0,0,0]
	v_mfma_scale_f32_16x16x128_f8f6f4 v[66:69], v[10:17], v[30:37], v[66:69], v232, v232 op_sel_hi:[0,0,0]
	v_mfma_scale_f32_16x16x128_f8f6f4 v[62:65], v[2:9], v[38:45], v[62:65], v232, v232 op_sel_hi:[0,0,0]
	v_mfma_scale_f32_16x16x128_f8f6f4 v[58:61], v[10:17], v[38:45], v[58:61], v232, v232 op_sel_hi:[0,0,0]
	v_mfma_scale_f32_16x16x128_f8f6f4 v[54:57], v[2:9], v[82:89], v[54:57], v232, v232 op_sel_hi:[0,0,0]
	v_mfma_scale_f32_16x16x128_f8f6f4 v[50:53], v[10:17], v[82:89], v[50:53], v232, v232 op_sel_hi:[0,0,0]
	s_setprio 0
	s_barrier
	v_mov_b32_e32 v95, v219
	v_lshl_add_u64 v[92:93], s[26:27], 0, v[94:95]
	v_mov_b32_e32 v99, v219
	s_mov_b32 m0, s40
	v_lshl_add_u64 v[30:31], v[92:93], 0, s[76:77]
	v_lshl_add_u64 v[180:181], s[26:27], 0, v[98:99]
	ds_read_b128 v[22:25], v183 offset:16384
	ds_read_b128 v[26:29], v183 offset:17408
	ds_read_b128 v[82:85], v183 offset:18432
	ds_read_b128 v[86:89], v183 offset:19456
	ds_read_b128 v[164:167], v183 offset:20480
	ds_read_b128 v[168:171], v183 offset:21504
	ds_read_b128 v[172:175], v183 offset:22528
	ds_read_b128 v[176:179], v183 offset:23552
	global_load_lds_dwordx4 v[30:31], off
	v_lshl_add_u64 v[32:33], v[180:181], 0, s[76:77]
	s_mov_b32 m0, s41
	v_lshl_add_u64 v[192:193], s[24:25], 0, v[218:219]
	global_load_lds_dwordx4 v[32:33], off
	v_lshl_add_u64 v[194:195], s[24:25], 0, v[96:97]
	v_lshl_add_u64 v[30:31], v[192:193], 0, s[76:77]
	s_mov_b32 m0, s44
	s_add_u32 s6, s24, 0x10100
	global_load_lds_dwordx4 v[30:31], off
	v_lshl_add_u64 v[30:31], v[194:195], 0, s[76:77]
	s_mov_b32 m0, s45
	s_addc_u32 s7, s25, 0
	global_load_lds_dwordx4 v[30:31], off
	s_waitcnt vmcnt(6)
	s_waitcnt lgkmcnt(0)
	s_barrier
	s_setprio 1
	v_mov_b64_e32 v[46:47], s[88:89]
	v_mov_b64_e32 v[42:43], s[88:89]
	v_mov_b64_e32 v[48:49], s[90:91]
	v_mov_b64_e32 v[44:45], s[90:91]
	s_waitcnt lgkmcnt(0)
	v_mfma_scale_f32_16x16x128_f8f6f4 v[46:49], v[2:9], v[22:29], v[46:49], v232, v232 op_sel_hi:[0,0,0]
	v_mfma_scale_f32_16x16x128_f8f6f4 v[42:45], v[10:17], v[22:29], v[42:45], v232, v232 op_sel_hi:[0,0,0]
	v_mov_b64_e32 v[38:39], s[88:89]
	v_mov_b64_e32 v[34:35], s[88:89]
	v_mov_b64_e32 v[30:31], s[88:89]
	v_mov_b64_e32 v[26:27], s[88:89]
	v_mov_b64_e32 v[22:23], s[88:89]
	v_mov_b64_e32 v[40:41], s[90:91]
	v_mov_b64_e32 v[36:37], s[90:91]
	v_mov_b64_e32 v[32:33], s[90:91]
	v_mov_b64_e32 v[28:29], s[90:91]
	v_mov_b64_e32 v[24:25], s[90:91]
	v_mfma_scale_f32_16x16x128_f8f6f4 v[38:41], v[2:9], v[82:89], v[38:41], v232, v232 op_sel_hi:[0,0,0]
	v_mfma_scale_f32_16x16x128_f8f6f4 v[34:37], v[10:17], v[82:89], v[34:37], v232, v232 op_sel_hi:[0,0,0]
	v_mfma_scale_f32_16x16x128_f8f6f4 v[30:33], v[2:9], v[164:171], v[30:33], v232, v232 op_sel_hi:[0,0,0]
	v_mfma_scale_f32_16x16x128_f8f6f4 v[26:29], v[10:17], v[164:171], v[26:29], v232, v232 op_sel_hi:[0,0,0]
	v_mfma_scale_f32_16x16x128_f8f6f4 v[22:25], v[2:9], v[172:179], v[22:25], v232, v232 op_sel_hi:[0,0,0]
	v_mfma_scale_f32_16x16x128_f8f6f4 v[18:21], v[10:17], v[172:179], v[18:21], v232, v232 op_sel_hi:[0,0,0]
	s_setprio 0
	s_barrier
	v_add_u32_e32 v82, s48, v182
	ds_read_b128 v[2:5], v82
	ds_read_b128 v[6:9], v82 offset:1024
	ds_read_b128 v[10:13], v82 offset:2048
	ds_read_b128 v[14:17], v82 offset:3072
	s_mov_b32 m0, s46
	ds_read_b128 v[84:87], v183 offset:32768
	ds_read_b128 v[88:91], v183 offset:33792
	ds_read_b128 v[164:167], v183 offset:34816
	ds_read_b128 v[168:171], v183 offset:35840
	ds_read_b128 v[172:175], v183 offset:36864
	ds_read_b128 v[176:179], v183 offset:37888
	ds_read_b128 v[184:187], v183 offset:38912
	ds_read_b128 v[188:191], v183 offset:39936
	global_load_lds_dwordx4 v218, s[6:7]
	s_mov_b32 m0, s47
	s_nop 0
	global_load_lds_dwordx4 v96, s[6:7]
	s_waitcnt vmcnt(6)
	s_waitcnt lgkmcnt(0)
	s_barrier
	s_setprio 1
	s_waitcnt lgkmcnt(0)
	v_mfma_scale_f32_16x16x128_f8f6f4 v[78:81], v[2:9], v[84:91], v[78:81], v232, v232 op_sel_hi:[0,0,0]
	v_mfma_scale_f32_16x16x128_f8f6f4 v[74:77], v[10:17], v[84:91], v[74:77], v232, v232 op_sel_hi:[0,0,0]
	v_mfma_scale_f32_16x16x128_f8f6f4 v[70:73], v[2:9], v[164:171], v[70:73], v232, v232 op_sel_hi:[0,0,0]
	v_mfma_scale_f32_16x16x128_f8f6f4 v[66:69], v[10:17], v[164:171], v[66:69], v232, v232 op_sel_hi:[0,0,0]
	v_mfma_scale_f32_16x16x128_f8f6f4 v[62:65], v[2:9], v[172:179], v[62:65], v232, v232 op_sel_hi:[0,0,0]
	v_mfma_scale_f32_16x16x128_f8f6f4 v[58:61], v[10:17], v[172:179], v[58:61], v232, v232 op_sel_hi:[0,0,0]
	v_mfma_scale_f32_16x16x128_f8f6f4 v[54:57], v[2:9], v[184:191], v[54:57], v232, v232 op_sel_hi:[0,0,0]
	v_mfma_scale_f32_16x16x128_f8f6f4 v[50:53], v[10:17], v[184:191], v[50:53], v232, v232 op_sel_hi:[0,0,0]
	s_setprio 0
	s_barrier
	s_mov_b64 s[6:7], 0x180
	s_mov_b32 m0, s49
	v_lshl_add_u64 v[92:93], v[92:93], 0, s[6:7]
	ds_read_b128 v[84:87], v183 offset:49152
	ds_read_b128 v[88:91], v183 offset:50176
	ds_read_b128 v[164:167], v183 offset:51200
	ds_read_b128 v[168:171], v183 offset:52224
	ds_read_b128 v[172:175], v183 offset:53248
	ds_read_b128 v[176:179], v183 offset:54272
	ds_read_b128 v[184:187], v183 offset:55296
	ds_read_b128 v[188:191], v183 offset:56320
	global_load_lds_dwordx4 v[92:93], off
	v_lshl_add_u64 v[180:181], v[180:181], 0, s[6:7]
	s_mov_b32 m0, s50
	s_nop 0
	global_load_lds_dwordx4 v[180:181], off
	s_nop 0
	v_lshl_add_u64 v[92:93], v[192:193], 0, s[6:7]
	s_mov_b32 m0, s51
	s_nop 0
	global_load_lds_dwordx4 v[92:93], off
	v_lshl_add_u64 v[92:93], v[194:195], 0, s[6:7]
	s_mov_b32 m0, s56
	s_nop 0
	global_load_lds_dwordx4 v[92:93], off
	s_waitcnt vmcnt(6)
	s_waitcnt lgkmcnt(0)
	s_barrier
	s_setprio 1
	s_waitcnt lgkmcnt(0)
	v_mfma_scale_f32_16x16x128_f8f6f4 v[46:49], v[2:9], v[84:91], v[46:49], v232, v232 op_sel_hi:[0,0,0]
	v_mfma_scale_f32_16x16x128_f8f6f4 v[42:45], v[10:17], v[84:91], v[42:45], v232, v232 op_sel_hi:[0,0,0]
	v_mfma_scale_f32_16x16x128_f8f6f4 v[38:41], v[2:9], v[164:171], v[38:41], v232, v232 op_sel_hi:[0,0,0]
	v_mfma_scale_f32_16x16x128_f8f6f4 v[34:37], v[10:17], v[164:171], v[34:37], v232, v232 op_sel_hi:[0,0,0]
	v_mfma_scale_f32_16x16x128_f8f6f4 v[30:33], v[2:9], v[172:179], v[30:33], v232, v232 op_sel_hi:[0,0,0]
	v_mfma_scale_f32_16x16x128_f8f6f4 v[26:29], v[10:17], v[172:179], v[26:29], v232, v232 op_sel_hi:[0,0,0]
	v_mfma_scale_f32_16x16x128_f8f6f4 v[22:25], v[2:9], v[184:191], v[22:25], v232, v232 op_sel_hi:[0,0,0]
	v_mfma_scale_f32_16x16x128_f8f6f4 v[18:21], v[10:17], v[184:191], v[18:21], v232, v232 op_sel_hi:[0,0,0]
	s_setprio 0
	s_barrier
	ds_read_b128 v[2:5], v196
	ds_read_b128 v[6:9], v196 offset:1024
	ds_read_b128 v[10:13], v196 offset:2048
	ds_read_b128 v[14:17], v196 offset:3072
	s_add_u32 s6, s24, 0x10180
	s_addc_u32 s7, s25, 0
	s_mov_b32 m0, s4
	ds_read_b128 v[84:87], v183
	ds_read_b128 v[88:91], v183 offset:1024
	ds_read_b128 v[164:167], v183 offset:2048
	ds_read_b128 v[168:171], v183 offset:3072
	ds_read_b128 v[172:175], v183 offset:4096
	ds_read_b128 v[176:179], v183 offset:5120
	ds_read_b128 v[184:187], v183 offset:6144
	ds_read_b128 v[188:191], v183 offset:7168
	global_load_lds_dwordx4 v218, s[6:7]
	s_mov_b32 m0, s5
	s_nop 0
	global_load_lds_dwordx4 v96, s[6:7]
	s_waitcnt vmcnt(6)
	s_waitcnt lgkmcnt(0)
	s_barrier
	s_setprio 1
	s_waitcnt lgkmcnt(0)
	v_mfma_scale_f32_16x16x128_f8f6f4 v[78:81], v[2:9], v[84:91], v[78:81], v232, v232 op_sel_hi:[0,0,0]
	v_mfma_scale_f32_16x16x128_f8f6f4 v[74:77], v[10:17], v[84:91], v[74:77], v232, v232 op_sel_hi:[0,0,0]
	v_mfma_scale_f32_16x16x128_f8f6f4 v[70:73], v[2:9], v[164:171], v[70:73], v232, v232 op_sel_hi:[0,0,0]
	v_mfma_scale_f32_16x16x128_f8f6f4 v[66:69], v[10:17], v[164:171], v[66:69], v232, v232 op_sel_hi:[0,0,0]
	v_mfma_scale_f32_16x16x128_f8f6f4 v[62:65], v[2:9], v[172:179], v[62:65], v232, v232 op_sel_hi:[0,0,0]
	v_mfma_scale_f32_16x16x128_f8f6f4 v[58:61], v[10:17], v[172:179], v[58:61], v232, v232 op_sel_hi:[0,0,0]
	v_mfma_scale_f32_16x16x128_f8f6f4 v[54:57], v[2:9], v[184:191], v[54:57], v232, v232 op_sel_hi:[0,0,0]
	v_mfma_scale_f32_16x16x128_f8f6f4 v[50:53], v[10:17], v[184:191], v[50:53], v232, v232 op_sel_hi:[0,0,0]
	s_setprio 0
	s_barrier
	s_mul_i32 s4, s19, s28
	s_mul_hi_i32 s5, s19, s28
	s_add_u32 s4, s4, s29
	s_addc_u32 s5, s5, s60
	v_cmp_gt_i64_e32 vcc, s[4:5], v[252:253]
	v_cmp_lt_i64_e64 s[6:7], s[4:5], v[220:221]
	s_cbranch_vccnz .LBB0_878
	s_ashr_i32 s15, s4, 31
	s_lshr_b32 s15, s15, 29
	s_add_i32 s15, s4, s15
	s_ashr_i32 s16, s15, 3
	s_and_b32 s15, s15, -8
	s_sub_i32 s4, s4, s15
	s_lshr_b32 s15, s4, 31
	s_or_b32 s15, s15, 32
	s_mul_i32 s4, s15, s4
	s_add_i32 s16, s4, s16
	s_ashr_i32 s4, s16, 31
	s_lshr_b32 s4, s4, 27
	s_add_i32 s17, s16, s4
	s_mul_i32 s19, s19, 6
	s_ashr_i32 s4, s17, 5
	s_sub_i32 s5, s61, s19
	s_lshl_b32 s19, s4, 3
	s_sub_i32 s4, 64, s19
	s_min_i32 s20, s4, 8
	s_abs_i32 s21, s20
	v_cvt_f32_u32_e32 v83, s21
	s_mul_hi_u32 s14, s5, 0x55555556
	s_lshl_b32 s18, s14, 7
	s_mul_i32 s14, s14, -3
	v_rcp_iflag_f32_e32 v83, v83
	s_add_i32 s14, s5, s14
	s_sub_i32 s36, 0, s21
	s_ashr_i32 s15, s14, 31
	v_mul_f32_e32 v83, 0x4f7ffffe, v83
	v_cvt_u32_f32_e32 v83, v83
	s_andn2_b32 s17, s17, 31
	s_lshl_b64 s[4:5], s[14:15], 19
	s_sub_i32 s15, s16, s17
	v_readfirstlane_b32 s38, v83
	s_mul_i32 s36, s36, s38
	s_mul_hi_u32 s36, s38, s36
	s_abs_i32 s17, s15
	s_add_i32 s38, s38, s36
	s_mul_hi_u32 s36, s17, s38
	s_mul_i32 s38, s36, s21
	s_xor_b32 s16, s15, s20
	s_sub_i32 s17, s17, s38
	s_ashr_i32 s16, s16, 31
	s_add_i32 s38, s36, 1
	s_sub_i32 s52, s17, s21
	s_cmp_ge_u32 s17, s21
	s_cselect_b32 s36, s38, s36
	s_cselect_b32 s17, s52, s17
	s_add_i32 s38, s36, 1
	s_cmp_ge_u32 s17, s21
	s_cselect_b32 s17, s38, s36
	s_xor_b32 s17, s17, s16
	s_sub_i32 s21, s17, s16
	s_mul_i32 s16, s21, s20
	s_sub_i32 s15, s15, s16
	s_add_i32 s15, s15, s19
	s_cmp_gt_i32 s15, 31
	s_cselect_b32 s16, 2, 1
	s_add_i32 s52, s16, s15
	s_mul_i32 s16, s14, 0x1100000
	s_mul_hi_i32 s15, s14, 0x1100000
	s_add_u32 s19, s30, s16
	s_addc_u32 s15, s31, s15
	s_ashr_i32 s53, s52, 31
	s_lshl_b64 s[16:17], s[52:53], 17
	s_add_u32 s16, s19, s16
	s_addc_u32 s17, s15, s17
	s_add_u32 s15, s34, s4
	s_addc_u32 s36, s35, s5
	s_lshl_b32 s4, s21, 8
	s_add_i32 s18, s4, s18
	s_ashr_i32 s19, s18, 31
	s_lshl_b64 s[4:5], s[18:19], 9
	s_add_u32 s20, s15, s4
	s_mov_b32 s97, 0x100000
	s_addc_u32 s21, s36, s5
	s_lshl_b32 s15, s52, 8
	s_movk_i32 s96, 0x1000

.LBB0_880:
	s_mov_b32 m0, s40
	v_lshl_add_u64 v[92:93], s[26:27], 0, v[94:95]
	ds_read_b128 v[84:87], v183 offset:16384
	ds_read_b128 v[88:91], v183 offset:17408
	ds_read_b128 v[164:167], v183 offset:18432
	ds_read_b128 v[168:171], v183 offset:19456
	ds_read_b128 v[172:175], v183 offset:20480
	ds_read_b128 v[176:179], v183 offset:21504
	ds_read_b128 v[184:187], v183 offset:22528
	ds_read_b128 v[188:191], v183 offset:23552
	global_load_lds_dwordx4 v[92:93], off
	v_lshl_add_u64 v[180:181], s[26:27], 0, v[98:99]
	s_mov_b32 m0, s41
	v_lshl_add_u64 v[192:193], s[24:25], 0, v[218:219]
	global_load_lds_dwordx4 v[180:181], off
	v_lshl_add_u64 v[194:195], s[24:25], 0, v[96:97]
	s_add_u32 s6, s24, 0x10000
	s_mov_b32 m0, s44
	s_addc_u32 s7, s25, 0
	global_load_lds_dwordx4 v[192:193], off
	s_mov_b32 m0, s45
	s_nop 0
	global_load_lds_dwordx4 v[194:195], off
	s_waitcnt vmcnt(6)
	s_waitcnt lgkmcnt(0)
	s_barrier
	s_setprio 1
	s_waitcnt lgkmcnt(0)
	v_mfma_scale_f32_16x16x128_f8f6f4 v[46:49], v[2:9], v[84:91], v[46:49], v232, v232 op_sel_hi:[0,0,0]
	v_mfma_scale_f32_16x16x128_f8f6f4 v[42:45], v[10:17], v[84:91], v[42:45], v232, v232 op_sel_hi:[0,0,0]
	v_mfma_scale_f32_16x16x128_f8f6f4 v[38:41], v[2:9], v[164:171], v[38:41], v232, v232 op_sel_hi:[0,0,0]
	v_mfma_scale_f32_16x16x128_f8f6f4 v[34:37], v[10:17], v[164:171], v[34:37], v232, v232 op_sel_hi:[0,0,0]
	v_mfma_scale_f32_16x16x128_f8f6f4 v[30:33], v[2:9], v[172:179], v[30:33], v232, v232 op_sel_hi:[0,0,0]
	v_mfma_scale_f32_16x16x128_f8f6f4 v[26:29], v[10:17], v[172:179], v[26:29], v232, v232 op_sel_hi:[0,0,0]
	v_mfma_scale_f32_16x16x128_f8f6f4 v[22:25], v[2:9], v[184:191], v[22:25], v232, v232 op_sel_hi:[0,0,0]
	v_mfma_scale_f32_16x16x128_f8f6f4 v[18:21], v[10:17], v[184:191], v[18:21], v232, v232 op_sel_hi:[0,0,0]
	s_setprio 0
	s_barrier
	ds_read_b128 v[2:5], v82
	ds_read_b128 v[6:9], v82 offset:1024
	ds_read_b128 v[10:13], v82 offset:2048
	ds_read_b128 v[14:17], v82 offset:3072
	s_mov_b32 m0, s46
	v_lshl_add_u64 v[90:91], s[6:7], 0, v[218:219]
	ds_read_b128 v[82:85], v183 offset:32768
	ds_read_b128 v[86:89], v183 offset:33792
	ds_read_b128 v[164:167], v183 offset:34816
	ds_read_b128 v[168:171], v183 offset:35840
	ds_read_b128 v[172:175], v183 offset:36864
	ds_read_b128 v[176:179], v183 offset:37888
	ds_read_b128 v[184:187], v183 offset:38912
	ds_read_b128 v[188:191], v183 offset:39936
	global_load_lds_dwordx4 v[90:91], off
	v_lshl_add_u64 v[90:91], s[6:7], 0, v[96:97]
	s_mov_b32 m0, s47
	s_nop 0
	global_load_lds_dwordx4 v[90:91], off
	s_waitcnt vmcnt(6)
	s_waitcnt lgkmcnt(0)
	s_barrier
	s_setprio 1
	s_waitcnt lgkmcnt(0)
	v_mfma_scale_f32_16x16x128_f8f6f4 v[78:81], v[2:9], v[82:89], v[78:81], v232, v232 op_sel_hi:[0,0,0]
	v_mfma_scale_f32_16x16x128_f8f6f4 v[74:77], v[10:17], v[82:89], v[74:77], v232, v232 op_sel_hi:[0,0,0]
	v_mfma_scale_f32_16x16x128_f8f6f4 v[70:73], v[2:9], v[164:171], v[70:73], v232, v232 op_sel_hi:[0,0,0]
	v_mfma_scale_f32_16x16x128_f8f6f4 v[66:69], v[10:17], v[164:171], v[66:69], v232, v232 op_sel_hi:[0,0,0]
	v_mfma_scale_f32_16x16x128_f8f6f4 v[62:65], v[2:9], v[172:179], v[62:65], v232, v232 op_sel_hi:[0,0,0]
	v_mfma_scale_f32_16x16x128_f8f6f4 v[58:61], v[10:17], v[172:179], v[58:61], v232, v232 op_sel_hi:[0,0,0]
	v_mfma_scale_f32_16x16x128_f8f6f4 v[54:57], v[2:9], v[184:191], v[54:57], v232, v232 op_sel_hi:[0,0,0]
	v_mfma_scale_f32_16x16x128_f8f6f4 v[50:53], v[10:17], v[184:191], v[50:53], v232, v232 op_sel_hi:[0,0,0]
	s_setprio 0
	s_barrier
	s_mov_b32 m0, s49
	v_lshl_add_u64 v[90:91], v[92:93], 0, s[72:73]
	ds_read_b128 v[82:85], v183 offset:49152
	ds_read_b128 v[86:89], v183 offset:50176
	ds_read_b128 v[164:167], v183 offset:51200
	ds_read_b128 v[168:171], v183 offset:52224
	ds_read_b128 v[172:175], v183 offset:53248
	ds_read_b128 v[176:179], v183 offset:54272
	ds_read_b128 v[184:187], v183 offset:55296
	ds_read_b128 v[188:191], v183 offset:56320
	global_load_lds_dwordx4 v[90:91], off
	v_lshl_add_u64 v[92:93], v[180:181], 0, s[72:73]
	s_mov_b32 m0, s50
	s_nop 0
	global_load_lds_dwordx4 v[92:93], off
	s_nop 0
	v_lshl_add_u64 v[90:91], v[192:193], 0, s[72:73]
	s_mov_b32 m0, s51
	s_nop 0
	global_load_lds_dwordx4 v[90:91], off
	v_lshl_add_u64 v[90:91], v[194:195], 0, s[72:73]
	s_mov_b32 m0, s56
	s_nop 0
	global_load_lds_dwordx4 v[90:91], off
	s_waitcnt vmcnt(6)
	s_waitcnt lgkmcnt(0)
	s_barrier
	s_setprio 1
	s_waitcnt lgkmcnt(0)
	v_mfma_scale_f32_16x16x128_f8f6f4 v[46:49], v[2:9], v[82:89], v[46:49], v232, v232 op_sel_hi:[0,0,0]
	v_mfma_scale_f32_16x16x128_f8f6f4 v[42:45], v[10:17], v[82:89], v[42:45], v232, v232 op_sel_hi:[0,0,0]
	v_mfma_scale_f32_16x16x128_f8f6f4 v[38:41], v[2:9], v[164:171], v[38:41], v232, v232 op_sel_hi:[0,0,0]
	v_mfma_scale_f32_16x16x128_f8f6f4 v[34:37], v[10:17], v[164:171], v[34:37], v232, v232 op_sel_hi:[0,0,0]
	v_mfma_scale_f32_16x16x128_f8f6f4 v[30:33], v[2:9], v[172:179], v[30:33], v232, v232 op_sel_hi:[0,0,0]
	v_mfma_scale_f32_16x16x128_f8f6f4 v[26:29], v[10:17], v[172:179], v[26:29], v232, v232 op_sel_hi:[0,0,0]
	v_mfma_scale_f32_16x16x128_f8f6f4 v[22:25], v[2:9], v[184:191], v[22:25], v232, v232 op_sel_hi:[0,0,0]
	v_mfma_scale_f32_16x16x128_f8f6f4 v[18:21], v[10:17], v[184:191], v[18:21], v232, v232 op_sel_hi:[0,0,0]
	s_setprio 0
	s_barrier
	s_andn2_b64 vcc, exec, s[12:13]
	s_cbranch_vccnz .LBB0_882
	s_barrier
